# R2 shared-expert silu epilogue re-emitted with 8 interleaved chains (bit-identical); header comment lists all E8M0 scales
# baseline (speedup 1.0000x reference)
; __device__ __forceinline__ unsigned pk2(float lo, float hi) { unsigned r; asm("v_cvt_pk_bf16_f32 %0, %1, %2" : "=v"(r) : "v"(lo), "v"(hi)); return r; }
; __device__ __forceinline__ float siluf_(float x) { return x * __builtin_amdgcn_rcpf(1.f + __expf(-x)); }
;     __device__ __forceinline__ void operator()(const f32x4 (&acc)[2][2][4][2], const Unit& u, int wr, int wc, int fr, int fq) const {
;     ...
;             const int col0 = (u.pn - 1) * 128 + wc * 32 + 8 * fq;
; #pragma unroll
;             for (int ai = 0; ai < 2; ++ai)
; #pragma unroll
;                 for (int m = 0; m < 4; ++m) { float o[8];
; #pragma unroll
;                     for (int n = 0; n < 2; ++n)
; #pragma unroll
;                         for (int i = 0; i < 4; ++i) o[n * 4 + i] = siluf_(acc[ai][0][m][n][i]) * acc[ai][1][m][n][i];
;                     v4u w; w.x = pk2(o[0], o[1]); w.y = pk2(o[2], o[3]); w.z = pk2(o[4], o[5]); w.w = pk2(o[6], o[7]);
;                     *(v4u*)(Act + (size_t)(row0 + ai * 128 + m * 16) * 256 + col0) = w; }
.LBB0_1055:
	v_lshl_add_u32 v148, s5, 8, v1
	v_or_b32_e32 v146, 16, v148
	v_or_b32_e32 v144, 32, v148
	v_or_b32_e32 v142, 48, v148
	s_cmp_lg_u32 s4, 0
	v_ashrrev_i32_e32 v149, 31, v148
	v_ashrrev_i32_e32 v147, 31, v146
	v_ashrrev_i32_e32 v145, 31, v144
	v_ashrrev_i32_e32 v143, 31, v142
	s_movk_i32 s62, 0x2000
	s_movk_i32 s61, 0xdff
	s_cbranch_scc0 .LBB0_1061
	v_lshl_add_u32 v176, s4, 7, v151
	v_ashrrev_i32_e32 v177, 31, v176
	v_lshlrev_b64 v[176:177], 1, v[176:177]
	v_lshl_add_u64 v[176:177], s[6:7], 0, v[176:177]
	v_lshlrev_b64 v[178:179], 9, v[148:149]
	v_lshl_add_u64 v[178:179], v[176:177], 0, v[178:179]
	v_mul_f32_e32 v168, 0xbfb8aa3b, v66
	v_mul_f32_e32 v169, 0xbfb8aa3b, v67
	v_mul_f32_e32 v170, 0xbfb8aa3b, v68
	v_mul_f32_e32 v171, 0xbfb8aa3b, v69
	v_mul_f32_e32 v172, 0xbfb8aa3b, v62
	v_mul_f32_e32 v173, 0xbfb8aa3b, v63
	v_mul_f32_e32 v174, 0xbfb8aa3b, v64
	v_mul_f32_e32 v175, 0xbfb8aa3b, v65
	v_exp_f32_e32 v168, v168
	v_exp_f32_e32 v169, v169
	v_exp_f32_e32 v170, v170
	v_exp_f32_e32 v171, v171
	v_exp_f32_e32 v172, v172
	v_exp_f32_e32 v173, v173
	v_exp_f32_e32 v174, v174
	v_exp_f32_e32 v175, v175
	v_add_f32_e32 v168, 1.0, v168
	v_add_f32_e32 v169, 1.0, v169
	v_add_f32_e32 v170, 1.0, v170
	v_add_f32_e32 v171, 1.0, v171
	v_add_f32_e32 v172, 1.0, v172
	v_add_f32_e32 v173, 1.0, v173
	v_add_f32_e32 v174, 1.0, v174
	v_add_f32_e32 v175, 1.0, v175
	v_rcp_f32_e32 v168, v168
	v_rcp_f32_e32 v169, v169
	v_rcp_f32_e32 v170, v170
	v_rcp_f32_e32 v171, v171
	v_rcp_f32_e32 v172, v172
	v_rcp_f32_e32 v173, v173
	v_rcp_f32_e32 v174, v174
	v_rcp_f32_e32 v175, v175
	v_mul_f32_e32 v168, v66, v168
	v_mul_f32_e32 v169, v67, v169
	v_mul_f32_e32 v170, v68, v170
	v_mul_f32_e32 v171, v69, v171
	v_mul_f32_e32 v172, v62, v172
	v_mul_f32_e32 v173, v63, v173
	v_mul_f32_e32 v174, v64, v174
	v_mul_f32_e32 v175, v65, v175
	v_mul_f32_e32 v168, v168, v126
	v_mul_f32_e32 v169, v169, v127
	v_mul_f32_e32 v170, v170, v128
	v_mul_f32_e32 v171, v171, v129
	v_mul_f32_e32 v172, v172, v122
	v_mul_f32_e32 v173, v173, v123
	v_mul_f32_e32 v174, v174, v124
	v_mul_f32_e32 v175, v175, v125
	v_cvt_pk_bf16_f32 v168, v168, v169
	v_cvt_pk_bf16_f32 v169, v170, v171
	v_cvt_pk_bf16_f32 v170, v172, v173
	v_cvt_pk_bf16_f32 v171, v174, v175
	global_store_dwordx4 v[178:179], v[168:171], off
	v_mul_f32_e32 v184, 0xbfb8aa3b, v58
	v_mul_f32_e32 v185, 0xbfb8aa3b, v59
	v_mul_f32_e32 v186, 0xbfb8aa3b, v60
	v_mul_f32_e32 v187, 0xbfb8aa3b, v61
	v_mul_f32_e32 v188, 0xbfb8aa3b, v54
	v_mul_f32_e32 v189, 0xbfb8aa3b, v55
	v_mul_f32_e32 v190, 0xbfb8aa3b, v56
	v_mul_f32_e32 v191, 0xbfb8aa3b, v57
	v_exp_f32_e32 v184, v184
	v_exp_f32_e32 v185, v185
	v_exp_f32_e32 v186, v186
	v_exp_f32_e32 v187, v187
	v_exp_f32_e32 v188, v188
	v_exp_f32_e32 v189, v189
	v_exp_f32_e32 v190, v190
	v_exp_f32_e32 v191, v191
	v_lshlrev_b64 v[180:181], 9, v[146:147]
	v_lshl_add_u64 v[180:181], v[176:177], 0, v[180:181]
	v_add_f32_e32 v184, 1.0, v184
	v_add_f32_e32 v185, 1.0, v185
	v_add_f32_e32 v186, 1.0, v186
	v_add_f32_e32 v187, 1.0, v187
	v_add_f32_e32 v188, 1.0, v188
	v_add_f32_e32 v189, 1.0, v189
	v_add_f32_e32 v190, 1.0, v190
	v_add_f32_e32 v191, 1.0, v191
	v_rcp_f32_e32 v184, v184
	v_rcp_f32_e32 v185, v185
	v_rcp_f32_e32 v186, v186
	v_rcp_f32_e32 v187, v187
	v_rcp_f32_e32 v188, v188
	v_rcp_f32_e32 v189, v189
	v_rcp_f32_e32 v190, v190
	v_rcp_f32_e32 v191, v191
	v_mul_f32_e32 v184, v58, v184
	v_mul_f32_e32 v185, v59, v185
	v_mul_f32_e32 v186, v60, v186
	v_mul_f32_e32 v187, v61, v187
	v_mul_f32_e32 v188, v54, v188
	v_mul_f32_e32 v189, v55, v189
	v_mul_f32_e32 v190, v56, v190
	v_mul_f32_e32 v191, v57, v191
	v_mul_f32_e32 v184, v184, v118
	v_mul_f32_e32 v185, v185, v119
	v_mul_f32_e32 v186, v186, v120
	v_mul_f32_e32 v187, v187, v121
	v_mul_f32_e32 v188, v188, v114
	v_mul_f32_e32 v189, v189, v115
	v_mul_f32_e32 v190, v190, v116
	v_mul_f32_e32 v191, v191, v117
	v_cvt_pk_bf16_f32 v184, v184, v185
	v_cvt_pk_bf16_f32 v185, v186, v187
	v_cvt_pk_bf16_f32 v186, v188, v189
	v_cvt_pk_bf16_f32 v187, v190, v191
	global_store_dwordx4 v[180:181], v[184:187], off
	v_mul_f32_e32 v168, 0xbfb8aa3b, v50
	v_mul_f32_e32 v169, 0xbfb8aa3b, v51
	v_mul_f32_e32 v170, 0xbfb8aa3b, v52
	v_mul_f32_e32 v171, 0xbfb8aa3b, v53
	v_mul_f32_e32 v172, 0xbfb8aa3b, v46
	v_mul_f32_e32 v173, 0xbfb8aa3b, v47
	v_mul_f32_e32 v174, 0xbfb8aa3b, v48
	v_mul_f32_e32 v175, 0xbfb8aa3b, v49
	v_exp_f32_e32 v168, v168
	v_exp_f32_e32 v169, v169
	v_exp_f32_e32 v170, v170
	v_exp_f32_e32 v171, v171
	v_exp_f32_e32 v172, v172
	v_exp_f32_e32 v173, v173
	v_exp_f32_e32 v174, v174
	v_exp_f32_e32 v175, v175
	v_lshlrev_b64 v[182:183], 9, v[144:145]
	v_lshl_add_u64 v[182:183], v[176:177], 0, v[182:183]
	v_add_f32_e32 v168, 1.0, v168
	v_add_f32_e32 v169, 1.0, v169
	v_add_f32_e32 v170, 1.0, v170
	v_add_f32_e32 v171, 1.0, v171
	v_add_f32_e32 v172, 1.0, v172
	v_add_f32_e32 v173, 1.0, v173
	v_add_f32_e32 v174, 1.0, v174
	v_add_f32_e32 v175, 1.0, v175
	v_rcp_f32_e32 v168, v168
	v_rcp_f32_e32 v169, v169
	v_rcp_f32_e32 v170, v170
	v_rcp_f32_e32 v171, v171
	v_rcp_f32_e32 v172, v172
	v_rcp_f32_e32 v173, v173
	v_rcp_f32_e32 v174, v174
	v_rcp_f32_e32 v175, v175
	v_mul_f32_e32 v168, v50, v168
	v_mul_f32_e32 v169, v51, v169
	v_mul_f32_e32 v170, v52, v170
	v_mul_f32_e32 v171, v53, v171
	v_mul_f32_e32 v172, v46, v172
	v_mul_f32_e32 v173, v47, v173
	v_mul_f32_e32 v174, v48, v174
	v_mul_f32_e32 v175, v49, v175
	v_mul_f32_e32 v168, v168, v110
	v_mul_f32_e32 v169, v169, v111
	v_mul_f32_e32 v170, v170, v112
	v_mul_f32_e32 v171, v171, v113
	v_mul_f32_e32 v172, v172, v106
	v_mul_f32_e32 v173, v173, v107
	v_mul_f32_e32 v174, v174, v108
	v_mul_f32_e32 v175, v175, v109
	v_cvt_pk_bf16_f32 v168, v168, v169
	v_cvt_pk_bf16_f32 v169, v170, v171
; __device__ __forceinline__ unsigned pk2(float lo, float hi) { unsigned r; asm("v_cvt_pk_bf16_f32 %0, %1, %2" : "=v"(r) : "v"(lo), "v"(hi)); return r; }
; __device__ __forceinline__ float siluf_(float x) { return x * __builtin_amdgcn_rcpf(1.f + __expf(-x)); }
;     __device__ __forceinline__ void operator()(const f32x4 (&acc)[2][2][4][2], const Unit& u, int wr, int wc, int fr, int fq) const {
;     ...
;             const int col0 = (u.pn - 1) * 128 + wc * 32 + 8 * fq;
; #pragma unroll
;             for (int ai = 0; ai < 2; ++ai)
; #pragma unroll
;                 for (int m = 0; m < 4; ++m) { float o[8];
; #pragma unroll
;                     for (int n = 0; n < 2; ++n)
; #pragma unroll
;                         for (int i = 0; i < 4; ++i) o[n * 4 + i] = siluf_(acc[ai][0][m][n][i]) * acc[ai][1][m][n][i];
;                     v4u w; w.x = pk2(o[0], o[1]); w.y = pk2(o[2], o[3]); w.z = pk2(o[4], o[5]); w.w = pk2(o[6], o[7]);
;                     *(v4u*)(Act + (size_t)(row0 + ai * 128 + m * 16) * 256 + col0) = w; }
	v_cvt_pk_bf16_f32 v170, v172, v173
	v_cvt_pk_bf16_f32 v171, v174, v175
	global_store_dwordx4 v[182:183], v[168:171], off
	v_mul_f32_e32 v184, 0xbfb8aa3b, v42
	v_mul_f32_e32 v185, 0xbfb8aa3b, v43
	v_mul_f32_e32 v186, 0xbfb8aa3b, v44
	v_mul_f32_e32 v187, 0xbfb8aa3b, v45
	v_mul_f32_e32 v188, 0xbfb8aa3b, v38
	v_mul_f32_e32 v189, 0xbfb8aa3b, v39
	v_mul_f32_e32 v190, 0xbfb8aa3b, v40
	v_mul_f32_e32 v191, 0xbfb8aa3b, v41
	v_exp_f32_e32 v184, v184
	v_exp_f32_e32 v185, v185
	v_exp_f32_e32 v186, v186
	v_exp_f32_e32 v187, v187
	v_exp_f32_e32 v188, v188
	v_exp_f32_e32 v189, v189
	v_exp_f32_e32 v190, v190
	v_exp_f32_e32 v191, v191
	v_lshlrev_b64 v[192:193], 9, v[142:143]
	v_lshl_add_u64 v[192:193], v[176:177], 0, v[192:193]
	v_add_f32_e32 v184, 1.0, v184
	v_add_f32_e32 v185, 1.0, v185
	v_add_f32_e32 v186, 1.0, v186
	v_add_f32_e32 v187, 1.0, v187
	v_add_f32_e32 v188, 1.0, v188
	v_add_f32_e32 v189, 1.0, v189
	v_add_f32_e32 v190, 1.0, v190
	v_add_f32_e32 v191, 1.0, v191
	v_rcp_f32_e32 v184, v184
	v_rcp_f32_e32 v185, v185
	v_rcp_f32_e32 v186, v186
	v_rcp_f32_e32 v187, v187
	v_rcp_f32_e32 v188, v188
	v_rcp_f32_e32 v189, v189
	v_rcp_f32_e32 v190, v190
	v_rcp_f32_e32 v191, v191
	v_mul_f32_e32 v184, v42, v184
	v_mul_f32_e32 v185, v43, v185
	v_mul_f32_e32 v186, v44, v186
	v_mul_f32_e32 v187, v45, v187
	v_mul_f32_e32 v188, v38, v188
	v_mul_f32_e32 v189, v39, v189
	v_mul_f32_e32 v190, v40, v190
	v_mul_f32_e32 v191, v41, v191
	v_mul_f32_e32 v184, v184, v102
	v_mul_f32_e32 v185, v185, v103
	v_mul_f32_e32 v186, v186, v104
	v_mul_f32_e32 v187, v187, v105
	v_mul_f32_e32 v188, v188, v98
	v_mul_f32_e32 v189, v189, v99
	v_mul_f32_e32 v190, v190, v100
	v_mul_f32_e32 v191, v191, v101
	v_cvt_pk_bf16_f32 v184, v184, v185
	v_cvt_pk_bf16_f32 v185, v186, v187
	v_cvt_pk_bf16_f32 v186, v188, v189
	v_cvt_pk_bf16_f32 v187, v190, v191
	global_store_dwordx4 v[192:193], v[184:187], off
	v_mul_f32_e32 v168, 0xbfb8aa3b, v34
	v_mul_f32_e32 v169, 0xbfb8aa3b, v35
	v_mul_f32_e32 v170, 0xbfb8aa3b, v36
	v_mul_f32_e32 v171, 0xbfb8aa3b, v37
	v_mul_f32_e32 v172, 0xbfb8aa3b, v26
	v_mul_f32_e32 v173, 0xbfb8aa3b, v27
	v_mul_f32_e32 v174, 0xbfb8aa3b, v28
	v_mul_f32_e32 v175, 0xbfb8aa3b, v29
	v_exp_f32_e32 v168, v168
	v_exp_f32_e32 v169, v169
	v_exp_f32_e32 v170, v170
	v_exp_f32_e32 v171, v171
	v_exp_f32_e32 v172, v172
	v_exp_f32_e32 v173, v173
	v_exp_f32_e32 v174, v174
	v_exp_f32_e32 v175, v175
	s_mov_b64 s[4:5], 0x10000
	v_lshl_add_u64 v[194:195], v[178:179], 0, s[4:5]
	v_add_f32_e32 v168, 1.0, v168
	v_add_f32_e32 v169, 1.0, v169
	v_add_f32_e32 v170, 1.0, v170
	v_add_f32_e32 v171, 1.0, v171
	v_add_f32_e32 v172, 1.0, v172
	v_add_f32_e32 v173, 1.0, v173
	v_add_f32_e32 v174, 1.0, v174
	v_add_f32_e32 v175, 1.0, v175
	v_rcp_f32_e32 v168, v168
	v_rcp_f32_e32 v169, v169
	v_rcp_f32_e32 v170, v170
	v_rcp_f32_e32 v171, v171
	v_rcp_f32_e32 v172, v172
	v_rcp_f32_e32 v173, v173
	v_rcp_f32_e32 v174, v174
	v_rcp_f32_e32 v175, v175
	v_mul_f32_e32 v168, v34, v168
	v_mul_f32_e32 v169, v35, v169
	v_mul_f32_e32 v170, v36, v170
	v_mul_f32_e32 v171, v37, v171
	v_mul_f32_e32 v172, v26, v172
	v_mul_f32_e32 v173, v27, v173
	v_mul_f32_e32 v174, v28, v174
	v_mul_f32_e32 v175, v29, v175
	v_mul_f32_e32 v168, v168, v94
	v_mul_f32_e32 v169, v169, v95
	v_mul_f32_e32 v170, v170, v96
	v_mul_f32_e32 v171, v171, v97
	v_mul_f32_e32 v172, v172, v90
	v_mul_f32_e32 v173, v173, v91
	v_mul_f32_e32 v174, v174, v92
	v_mul_f32_e32 v175, v175, v93
	v_cvt_pk_bf16_f32 v168, v168, v169
	v_cvt_pk_bf16_f32 v169, v170, v171
	v_cvt_pk_bf16_f32 v170, v172, v173
	v_cvt_pk_bf16_f32 v171, v174, v175
	global_store_dwordx4 v[194:195], v[168:171], off
	v_mul_f32_e32 v184, 0xbfb8aa3b, v22
	v_mul_f32_e32 v185, 0xbfb8aa3b, v23
	v_mul_f32_e32 v186, 0xbfb8aa3b, v24
	v_mul_f32_e32 v187, 0xbfb8aa3b, v25
	v_mul_f32_e32 v188, 0xbfb8aa3b, v18
	v_mul_f32_e32 v189, 0xbfb8aa3b, v19
	v_mul_f32_e32 v190, 0xbfb8aa3b, v20
	v_mul_f32_e32 v191, 0xbfb8aa3b, v21
	v_exp_f32_e32 v184, v184
	v_exp_f32_e32 v185, v185
	v_exp_f32_e32 v186, v186
	v_exp_f32_e32 v187, v187
	v_exp_f32_e32 v188, v188
	v_exp_f32_e32 v189, v189
	v_exp_f32_e32 v190, v190
	v_exp_f32_e32 v191, v191
	s_mov_b64 s[4:5], 0x12000
	v_lshl_add_u64 v[180:181], v[178:179], 0, s[4:5]
	v_add_f32_e32 v184, 1.0, v184
	v_add_f32_e32 v185, 1.0, v185
	v_add_f32_e32 v186, 1.0, v186
	v_add_f32_e32 v187, 1.0, v187
	v_add_f32_e32 v188, 1.0, v188
	v_add_f32_e32 v189, 1.0, v189
	v_add_f32_e32 v190, 1.0, v190
; __device__ __forceinline__ unsigned pk2(float lo, float hi) { unsigned r; asm("v_cvt_pk_bf16_f32 %0, %1, %2" : "=v"(r) : "v"(lo), "v"(hi)); return r; }
; __device__ __forceinline__ float siluf_(float x) { return x * __builtin_amdgcn_rcpf(1.f + __expf(-x)); }
;     __device__ __forceinline__ void operator()(const f32x4 (&acc)[2][2][4][2], const Unit& u, int wr, int wc, int fr, int fq) const {
;     ...
;             const int col0 = (u.pn - 1) * 128 + wc * 32 + 8 * fq;
; #pragma unroll
;             for (int ai = 0; ai < 2; ++ai)
; #pragma unroll
;                 for (int m = 0; m < 4; ++m) { float o[8];
; #pragma unroll
;                     for (int n = 0; n < 2; ++n)
; #pragma unroll
;                         for (int i = 0; i < 4; ++i) o[n * 4 + i] = siluf_(acc[ai][0][m][n][i]) * acc[ai][1][m][n][i];
;                     v4u w; w.x = pk2(o[0], o[1]); w.y = pk2(o[2], o[3]); w.z = pk2(o[4], o[5]); w.w = pk2(o[6], o[7]);
;                     *(v4u*)(Act + (size_t)(row0 + ai * 128 + m * 16) * 256 + col0) = w; }
	v_add_f32_e32 v191, 1.0, v191
	v_rcp_f32_e32 v184, v184
	v_rcp_f32_e32 v185, v185
	v_rcp_f32_e32 v186, v186
	v_rcp_f32_e32 v187, v187
	v_rcp_f32_e32 v188, v188
	v_rcp_f32_e32 v189, v189
	v_rcp_f32_e32 v190, v190
	v_rcp_f32_e32 v191, v191
	v_mul_f32_e32 v184, v22, v184
	v_mul_f32_e32 v185, v23, v185
	v_mul_f32_e32 v186, v24, v186
	v_mul_f32_e32 v187, v25, v187
	v_mul_f32_e32 v188, v18, v188
	v_mul_f32_e32 v189, v19, v189
	v_mul_f32_e32 v190, v20, v190
	v_mul_f32_e32 v191, v21, v191
	v_mul_f32_e32 v184, v184, v86
	v_mul_f32_e32 v185, v185, v87
	v_mul_f32_e32 v186, v186, v88
	v_mul_f32_e32 v187, v187, v89
	v_mul_f32_e32 v188, v188, v82
	v_mul_f32_e32 v189, v189, v83
	v_mul_f32_e32 v190, v190, v84
	v_mul_f32_e32 v191, v191, v85
	v_cvt_pk_bf16_f32 v184, v184, v185
	v_cvt_pk_bf16_f32 v185, v186, v187
	v_cvt_pk_bf16_f32 v186, v188, v189
	v_cvt_pk_bf16_f32 v187, v190, v191
	global_store_dwordx4 v[180:181], v[184:187], off
	v_mul_f32_e32 v168, 0xbfb8aa3b, v14
	v_mul_f32_e32 v169, 0xbfb8aa3b, v15
	v_mul_f32_e32 v170, 0xbfb8aa3b, v16
	v_mul_f32_e32 v171, 0xbfb8aa3b, v17
	v_mul_f32_e32 v172, 0xbfb8aa3b, v10
	v_mul_f32_e32 v173, 0xbfb8aa3b, v11
	v_mul_f32_e32 v174, 0xbfb8aa3b, v12
	v_mul_f32_e32 v175, 0xbfb8aa3b, v13
	v_exp_f32_e32 v168, v168
	v_exp_f32_e32 v169, v169
	v_exp_f32_e32 v170, v170
	v_exp_f32_e32 v171, v171
	v_exp_f32_e32 v172, v172
	v_exp_f32_e32 v173, v173
	v_exp_f32_e32 v174, v174
	v_exp_f32_e32 v175, v175
	s_mov_b64 s[4:5], 0x14000
	v_lshl_add_u64 v[182:183], v[178:179], 0, s[4:5]
	v_add_f32_e32 v168, 1.0, v168
	v_add_f32_e32 v169, 1.0, v169
	v_add_f32_e32 v170, 1.0, v170
	v_add_f32_e32 v171, 1.0, v171
	v_add_f32_e32 v172, 1.0, v172
	v_add_f32_e32 v173, 1.0, v173
	v_add_f32_e32 v174, 1.0, v174
	v_add_f32_e32 v175, 1.0, v175
	v_rcp_f32_e32 v168, v168
	v_rcp_f32_e32 v169, v169
	v_rcp_f32_e32 v170, v170
	v_rcp_f32_e32 v171, v171
	v_rcp_f32_e32 v172, v172
	v_rcp_f32_e32 v173, v173
	v_rcp_f32_e32 v174, v174
	v_rcp_f32_e32 v175, v175
	v_mul_f32_e32 v168, v14, v168
	v_mul_f32_e32 v169, v15, v169
	v_mul_f32_e32 v170, v16, v170
	v_mul_f32_e32 v171, v17, v171
	v_mul_f32_e32 v172, v10, v172
	v_mul_f32_e32 v173, v11, v173
	v_mul_f32_e32 v174, v12, v174
	v_mul_f32_e32 v175, v13, v175
	v_mul_f32_e32 v168, v168, v78
	v_mul_f32_e32 v169, v169, v79
	v_mul_f32_e32 v170, v170, v80
	v_mul_f32_e32 v171, v171, v81
	v_mul_f32_e32 v172, v172, v74
	v_mul_f32_e32 v173, v173, v75
	v_mul_f32_e32 v174, v174, v76
	v_mul_f32_e32 v175, v175, v77
	v_cvt_pk_bf16_f32 v168, v168, v169
	v_cvt_pk_bf16_f32 v169, v170, v171
	v_cvt_pk_bf16_f32 v170, v172, v173
	v_cvt_pk_bf16_f32 v171, v174, v175
	global_store_dwordx4 v[182:183], v[168:171], off
	v_mul_f32_e32 v184, 0xbfb8aa3b, v6
	v_mul_f32_e32 v185, 0xbfb8aa3b, v7
	v_mul_f32_e32 v186, 0xbfb8aa3b, v8
	v_mul_f32_e32 v187, 0xbfb8aa3b, v9
	v_mul_f32_e32 v188, 0xbfb8aa3b, v2
	v_mul_f32_e32 v189, 0xbfb8aa3b, v3
	v_mul_f32_e32 v190, 0xbfb8aa3b, v4
	v_mul_f32_e32 v191, 0xbfb8aa3b, v5
	v_exp_f32_e32 v184, v184
	v_exp_f32_e32 v185, v185
	v_exp_f32_e32 v186, v186
	v_exp_f32_e32 v187, v187
	v_exp_f32_e32 v188, v188
	v_exp_f32_e32 v189, v189
	v_exp_f32_e32 v190, v190
	v_exp_f32_e32 v191, v191
	s_mov_b64 s[4:5], 0x16000
	v_lshl_add_u64 v[192:193], v[178:179], 0, s[4:5]
	v_add_f32_e32 v184, 1.0, v184
	v_add_f32_e32 v185, 1.0, v185
	v_add_f32_e32 v186, 1.0, v186
	v_add_f32_e32 v187, 1.0, v187
	v_add_f32_e32 v188, 1.0, v188
	v_add_f32_e32 v189, 1.0, v189
	v_add_f32_e32 v190, 1.0, v190
	v_add_f32_e32 v191, 1.0, v191
	v_rcp_f32_e32 v184, v184
	v_rcp_f32_e32 v185, v185
	v_rcp_f32_e32 v186, v186
	v_rcp_f32_e32 v187, v187
	v_rcp_f32_e32 v188, v188
	v_rcp_f32_e32 v189, v189
	v_rcp_f32_e32 v190, v190
	v_rcp_f32_e32 v191, v191
	v_mul_f32_e32 v184, v6, v184
	v_mul_f32_e32 v185, v7, v185
	v_mul_f32_e32 v186, v8, v186
	v_mul_f32_e32 v187, v9, v187
	v_mul_f32_e32 v188, v2, v188
	v_mul_f32_e32 v189, v3, v189
	v_mul_f32_e32 v190, v4, v190
	v_mul_f32_e32 v191, v5, v191
	v_mul_f32_e32 v184, v184, v70
	v_mul_f32_e32 v185, v185, v71
	v_mul_f32_e32 v186, v186, v72
	v_mul_f32_e32 v187, v187, v73
	v_mul_f32_e32 v188, v188, v30
	v_mul_f32_e32 v189, v189, v31
	v_mul_f32_e32 v190, v190, v32
	v_mul_f32_e32 v191, v191, v33
	v_cvt_pk_bf16_f32 v184, v184, v185
	v_cvt_pk_bf16_f32 v185, v186, v187
	v_cvt_pk_bf16_f32 v186, v188, v189
	v_cvt_pk_bf16_f32 v187, v190, v191
	global_store_dwordx4 v[192:193], v[184:187], off
	s_mov_b32 s25, 0x38600000
	s_cbranch_execnz .LBB0_1058
